# v66 + ret_out P*V blocks: each transposed V fragment gets its own register quad, all LDS reads issued first, counted lgkmcnt per MFMA (was seven dependent LDS round trips per block)
# speedup vs baseline: 1.0135x; 1.0015x over previous
; #define MFMA16(a, b, c) __builtin_amdgcn_mfma_f32_16x16x32_bf16((a), (b), (c), 0, 0, 0)
; DI void ret_out_unit(const Ctx& c, int u) {
;     ...
;     for (int ks = 0; ks < 4; ++ks) if (ks <= (w >> 1)) { const bf16x8 pf = row_frag(Pimg, RS, 16 * w, ks * 32, lane);
; #pragma unroll
;         for (int ef = 0; ef < 8; ++ef) acc[ef] = MFMA16(tr_frag(Vimg, TS, ks * 32, ef * 16, lane), pf, acc[ef]); }
.LBB0_309:
	v_add_u32_e32 v64, v130, v78
	v_add_u32_e32 v66, v131, v78
	ds_read_b64_tr_b16 v[64:65], v64
	ds_read_b64_tr_b16 v[66:67], v66
	ds_read_b128 v[70:73], v82 offset:64
	v_add_u32_e32 v74, v130, v81
	v_add_u32_e32 v75, v131, v81
	ds_read_b64_tr_b16 v[106:107], v74
	v_add_u32_e32 v112, v130, v80
	v_add_u32_e32 v114, v131, v80
	ds_read_b64_tr_b16 v[108:109], v75
	ds_read_b64_tr_b16 v[112:113], v112
	ds_read_b64_tr_b16 v[114:115], v114
	v_add_u32_e32 v132, v130, v79
	v_add_u32_e32 v134, v131, v79
	ds_read_b64_tr_b16 v[132:133], v132
	ds_read_b64_tr_b16 v[134:135], v134
	v_add_u32_e32 v136, v130, v77
	v_add_u32_e32 v138, v131, v77
	ds_read_b64_tr_b16 v[136:137], v136
	ds_read_b64_tr_b16 v[138:139], v138
	v_add_u32_e32 v140, v130, v76
	v_add_u32_e32 v142, v131, v76
	ds_read_b64_tr_b16 v[140:141], v140
	ds_read_b64_tr_b16 v[142:143], v142
	v_add_u32_e32 v144, v130, v69
	v_add_u32_e32 v146, v131, v69
	ds_read_b64_tr_b16 v[144:145], v144
	ds_read_b64_tr_b16 v[146:147], v146
	v_add_u32_e32 v148, v130, v68
	v_add_u32_e32 v150, v131, v68
	ds_read_b64_tr_b16 v[148:149], v148
	ds_read_b64_tr_b16 v[150:151], v150
	s_waitcnt lgkmcnt(14)
	v_mfma_f32_16x16x32_bf16 v[60:63], v[64:67], v[70:73], v[60:63]
	s_waitcnt lgkmcnt(10)
	v_mfma_f32_16x16x32_bf16 v[52:55], v[112:115], v[70:73], v[52:55]
	s_waitcnt lgkmcnt(8)
	v_mfma_f32_16x16x32_bf16 v[48:51], v[132:135], v[70:73], v[48:51]
	s_waitcnt lgkmcnt(6)
	v_mfma_f32_16x16x32_bf16 v[44:47], v[136:139], v[70:73], v[44:47]
	s_waitcnt lgkmcnt(4)
	v_mfma_f32_16x16x32_bf16 v[40:43], v[140:143], v[70:73], v[40:43]
	s_waitcnt lgkmcnt(2)
	v_mfma_f32_16x16x32_bf16 v[36:39], v[144:147], v[70:73], v[36:39]
	s_waitcnt lgkmcnt(12)
	v_mfma_f32_16x16x32_bf16 v[56:59], v[106:109], v[70:73], v[56:59]
	s_waitcnt lgkmcnt(0)
	v_mfma_f32_16x16x32_bf16 v[32:35], v[148:151], v[70:73], v[32:35]
	s_and_b64 vcc, exec, s[6:7]
	s_cbranch_vccnz .LBB0_308
.LBB0_310:
	v_add_u32_e32 v64, v125, v78
	v_add_u32_e32 v66, v126, v78
	ds_read_b64_tr_b16 v[64:65], v64
	ds_read_b64_tr_b16 v[66:67], v66
	ds_read_b128 v[70:73], v82 offset:128
	v_add_u32_e32 v74, v125, v81
	v_add_u32_e32 v75, v126, v81
	ds_read_b64_tr_b16 v[106:107], v74
	v_add_u32_e32 v112, v125, v80
	v_add_u32_e32 v114, v126, v80
	ds_read_b64_tr_b16 v[108:109], v75
	ds_read_b64_tr_b16 v[112:113], v112
	ds_read_b64_tr_b16 v[114:115], v114
	v_add_u32_e32 v128, v125, v79
	v_add_u32_e32 v130, v126, v79
	ds_read_b64_tr_b16 v[128:129], v128
	ds_read_b64_tr_b16 v[130:131], v130
	v_add_u32_e32 v132, v125, v77
	v_add_u32_e32 v134, v126, v77
	ds_read_b64_tr_b16 v[132:133], v132
	ds_read_b64_tr_b16 v[134:135], v134
	v_add_u32_e32 v136, v125, v76
	v_add_u32_e32 v138, v126, v76
	ds_read_b64_tr_b16 v[136:137], v136
	ds_read_b64_tr_b16 v[138:139], v138
	v_add_u32_e32 v140, v125, v69
	v_add_u32_e32 v142, v126, v69
	ds_read_b64_tr_b16 v[140:141], v140
	ds_read_b64_tr_b16 v[142:143], v142
	v_add_u32_e32 v144, v125, v68
	v_add_u32_e32 v146, v126, v68
	ds_read_b64_tr_b16 v[144:145], v144
	ds_read_b64_tr_b16 v[146:147], v146
	s_waitcnt lgkmcnt(14)
	v_mfma_f32_16x16x32_bf16 v[60:63], v[64:67], v[70:73], v[60:63]
	s_waitcnt lgkmcnt(10)
	v_mfma_f32_16x16x32_bf16 v[52:55], v[112:115], v[70:73], v[52:55]
	s_waitcnt lgkmcnt(8)
	v_mfma_f32_16x16x32_bf16 v[48:51], v[128:131], v[70:73], v[48:51]
	s_waitcnt lgkmcnt(6)
	v_mfma_f32_16x16x32_bf16 v[44:47], v[132:135], v[70:73], v[44:47]
	s_waitcnt lgkmcnt(4)
	v_mfma_f32_16x16x32_bf16 v[40:43], v[136:139], v[70:73], v[40:43]
	s_waitcnt lgkmcnt(2)
	v_mfma_f32_16x16x32_bf16 v[36:39], v[140:143], v[70:73], v[36:39]
	s_waitcnt lgkmcnt(12)
	v_mfma_f32_16x16x32_bf16 v[56:59], v[106:109], v[70:73], v[56:59]
	s_waitcnt lgkmcnt(0)
	v_mfma_f32_16x16x32_bf16 v[32:35], v[144:147], v[70:73], v[32:35]
	s_and_b64 vcc, exec, s[8:9]
	s_lshl_b32 s6, s87, 7
	s_cbranch_vccnz .LBB0_272
.LBB0_311:
	v_add_u32_e32 v64, v105, v78
	v_add_u32_e32 v66, v124, v78
	ds_read_b64_tr_b16 v[64:65], v64
	ds_read_b64_tr_b16 v[66:67], v66
	ds_read_b128 v[70:73], v82 offset:192
	v_add_u32_e32 v74, v105, v81
	v_add_u32_e32 v75, v124, v81
	ds_read_b64_tr_b16 v[106:107], v74
	v_add_u32_e32 v112, v105, v80
	v_add_u32_e32 v114, v124, v80
	ds_read_b64_tr_b16 v[108:109], v75
	ds_read_b64_tr_b16 v[112:113], v112
	ds_read_b64_tr_b16 v[114:115], v114
	v_add_u32_e32 v128, v105, v79
	v_add_u32_e32 v130, v124, v79
	ds_read_b64_tr_b16 v[128:129], v128
	ds_read_b64_tr_b16 v[130:131], v130
	v_add_u32_e32 v132, v105, v77
	v_add_u32_e32 v134, v124, v77
	ds_read_b64_tr_b16 v[132:133], v132
	ds_read_b64_tr_b16 v[134:135], v134
	v_add_u32_e32 v136, v105, v76
	v_add_u32_e32 v138, v124, v76
	ds_read_b64_tr_b16 v[136:137], v136
	ds_read_b64_tr_b16 v[138:139], v138
	v_add_u32_e32 v140, v105, v69
	v_add_u32_e32 v142, v124, v69
	ds_read_b64_tr_b16 v[140:141], v140
	ds_read_b64_tr_b16 v[142:143], v142
	v_add_u32_e32 v144, v105, v68
	v_add_u32_e32 v146, v124, v68
	ds_read_b64_tr_b16 v[144:145], v144
	ds_read_b64_tr_b16 v[146:147], v146
	s_waitcnt lgkmcnt(14)
	v_mfma_f32_16x16x32_bf16 v[60:63], v[64:67], v[70:73], v[60:63]
	s_waitcnt lgkmcnt(10)
	v_mfma_f32_16x16x32_bf16 v[52:55], v[112:115], v[70:73], v[52:55]
	s_waitcnt lgkmcnt(8)
	v_mfma_f32_16x16x32_bf16 v[48:51], v[128:131], v[70:73], v[48:51]
	s_waitcnt lgkmcnt(6)
	v_mfma_f32_16x16x32_bf16 v[44:47], v[132:135], v[70:73], v[44:47]
	s_waitcnt lgkmcnt(4)
	v_mfma_f32_16x16x32_bf16 v[40:43], v[136:139], v[70:73], v[40:43]
	s_waitcnt lgkmcnt(2)
	v_mfma_f32_16x16x32_bf16 v[36:39], v[140:143], v[70:73], v[36:39]
	s_waitcnt lgkmcnt(12)
	v_mfma_f32_16x16x32_bf16 v[56:59], v[106:109], v[70:73], v[56:59]
	s_waitcnt lgkmcnt(0)
	v_mfma_f32_16x16x32_bf16 v[32:35], v[144:147], v[70:73], v[32:35]
	s_branch .LBB0_272
